# speedup vs baseline: 1.0304x; 1.0304x over previous
_Z11gram_kernelPKfPKiS0_S0_S0_S0_S0_S0_S0_S0_S0_Pf:
	s_load_dwordx4 s[24:27], s[0:1], 0x0
	s_load_dwordx2 s[28:29], s[0:1], 0x40
	s_load_dwordx4 s[20:23], s[0:1], 0x30
	s_load_dwordx2 s[10:11], s[0:1], 0x58
	s_load_dwordx2 s[44:45], s[0:1], 0x20
	s_load_dwordx2 s[68:69], s[0:1], 0x10
	s_load_dwordx2 s[60:61], s[0:1], 0x18
	s_load_dwordx2 s[62:63], s[0:1], 0x28
	s_load_dwordx2 s[64:65], s[0:1], 0x48
	s_load_dwordx2 s[66:67], s[0:1], 0x50
	s_ashr_i32 s30, s2, 1
	v_mov_b32_e32 v11, 0
	s_ashr_i32 s31, s30, 31
	s_lshl_b32 s46, s30, 11
	s_lshl_b32 s3, s2, 10
	s_ashr_i32 s47, s46, 31
	s_and_b32 s33, s3, 0x400
	v_lshlrev_b32_e32 v46, 2, v0
	v_mov_b32_e32 v47, 0
	v_lshlrev_b32_e32 v212, 1, v0
	v_mov_b32_e32 v213, v47
	v_lshrrev_b32_e32 v219, 6, v0
	v_bfe_u32 v214, v0, 5, 1
	v_and_b32_e32 v220, 31, v0
	s_or_b32 s3, s46, s33
	v_lshlrev_b32_e32 v216, 4, v219
	v_lshlrev_b32_e32 v221, 3, v214
	v_or3_b32 v1, s3, v216, v221
	v_lshlrev_b32_e32 v232, 4, v220
	v_and_b32_e32 v218, 63, v0
	s_mov_b32 s39, 0x20000
	s_brev_b32 s38, 16
	v_lshl_or_b32 v180, v1, 9, v232
	v_add_u32_e32 v1, 0x10000, v180
	s_lshl_b64 s[4:5], s[46:47], 2
	s_lshl_b32 s3, s33, 2
	s_lshl_b64 s[6:7], s[30:31], 14
	s_waitcnt lgkmcnt(0)
	s_add_u32 s48, s20, s6
	s_addc_u32 s49, s21, s7
	s_mov_b64 s[36:37], s[24:25]
	s_and_b32 s37, s37, 0xffff
	s_add_u32 s26, s26, s4
	s_addc_u32 s27, s27, s5
	s_add_u32 s26, s26, s3
	s_addc_u32 s27, s27, 0
	v_lshl_add_u64 v[32:33], v[212:213], 2, s[26:27]
	global_load_dwordx2 v[32:33], v[32:33], off
	buffer_load_dwordx4 v[34:37], v180, s[36:39], 0 offen nt
	buffer_load_dwordx4 v[38:41], v180, s[36:39], 0 offen offset:512 nt
	buffer_load_dwordx4 v[42:45], v180, s[36:39], 0 offen offset:1024 nt
	buffer_load_dwordx4 v[96:99], v180, s[36:39], 0 offen offset:1536 nt
	buffer_load_dwordx4 v[100:103], v180, s[36:39], 0 offen offset:2048 nt
	buffer_load_dwordx4 v[104:107], v180, s[36:39], 0 offen offset:2560 nt
	buffer_load_dwordx4 v[108:111], v180, s[36:39], 0 offen offset:3072 nt
	buffer_load_dwordx4 v[112:115], v180, s[36:39], 0 offen offset:3584 nt
	global_load_dword v250, v47, s[22:23]
	global_load_dword v250, v47, s[28:29]
	global_load_dword v250, v47, s[68:69]
	global_load_dword v250, v47, s[44:45]
	global_load_dword v250, v47, s[48:49]
	global_load_dword v250, v47, s[60:61]
	global_load_dword v250, v47, s[62:63]
	global_load_dword v250, v47, s[64:65]
	global_load_dword v250, v47, s[66:67]
	buffer_load_dwordx4 v[116:119], v1, s[36:39], 0 offen nt
	buffer_load_dwordx4 v[120:123], v1, s[36:39], 0 offen offset:512 nt
	buffer_load_dwordx4 v[124:127], v1, s[36:39], 0 offen offset:1024 nt
	buffer_load_dwordx4 v[128:131], v1, s[36:39], 0 offen offset:1536 nt
	buffer_load_dwordx4 v[132:135], v1, s[36:39], 0 offen offset:2048 nt
	buffer_load_dwordx4 v[136:139], v1, s[36:39], 0 offen offset:2560 nt
	buffer_load_dwordx4 v[140:143], v1, s[36:39], 0 offen offset:3072 nt
	buffer_load_dwordx4 v[144:147], v1, s[36:39], 0 offen offset:3584 nt
	s_movk_i32 s3, 0x160
	v_cmp_gt_u32_e32 vcc, s3, v0
	s_mov_b32 s3, 0x10000
	v_lshrrev_b32_e32 v227, 5, v0
	v_and_b32_e32 v228, 0x7c, v46
	v_add_u32_e32 v2, 0x200, v0
	v_lshrrev_b32_e32 v229, 5, v2
	v_mul_u32_u24_e32 v246, 0x110, v227
	v_lshl_add_u32 v246, v220, 3, v246
	v_add_u32_e32 v246, 0x10000, v246
	v_lshlrev_b32_e32 v247, 2, v46
	s_waitcnt vmcnt(25)
	v_cmp_ne_u32_e64 s[6:7], 0, v32
	v_cmp_ne_u32_e64 s[4:5], 0, v33
	v_cmp_eq_u32_e64 s[8:9], 0, v218
	s_nop 0
	s_and_saveexec_b64 s[12:13], s[8:9]
	s_cbranch_execz .LBB0_6
	s_bcnt1_i32_b64 s6, s[6:7]
	s_bcnt1_i32_b64 s4, s[4:5]
	v_mov_b32_e32 v1, 0x21100
	s_add_i32 s4, s4, s6
	v_lshl_add_u32 v1, v219, 2, v1
	v_mov_b32_e32 v2, s4
	ds_write_b32 v1, v2
.LBB0_6:
	s_or_b64 exec, exec, s[12:13]
	v_lshrrev_b32_e32 v222, 7, v0
	v_bfe_u32 v251, v0, 6, 2
	v_lshlrev_b32_e32 v215, 5, v251
	v_or_b32_e32 v231, v215, v220
	v_mul_u32_u24_e32 v224, 0x110, v231
	v_lshlrev_b32_e32 v223, 1, v221
	v_lshrrev_b32_e32 v225, 8, v0
	v_add3_u32 v248, v224, v223, s3
	s_waitcnt lgkmcnt(0)
	s_barrier
	s_movk_i32 s4, 0x110
	v_lshlrev_b32_e32 v230, 7, v225
	v_mad_u32_u24 v249, v231, s4, v230
	v_or_b32_e32 v249, v249, v221
	v_add_u32_e32 v249, 0x18800, v249
	v_mov_b32_e32 v1, 0x21100
	v_mov_b32_e32 v2, 0x21110
	ds_read_b128 v[6:9], v1
	ds_read_b128 v[2:5], v2
	s_mul_i32 s4, s2, 0x4590
	s_mul_hi_i32 s3, s2, 0x4590
	s_add_u32 s34, s10, s4
	s_addc_u32 s35, s11, s3
	s_and_saveexec_b64 s[4:5], vcc
	s_cbranch_execz .LBB0_8
	v_mov_b32_e32 v1, 0
	v_lshl_add_u64 v[12:13], v[0:1], 2, s[34:35]
	v_add_co_u32_e32 v12, vcc, 0x4000, v12
	s_nop 1
	v_addc_co_u32_e32 v13, vcc, 0, v13, vcc
	global_store_dword v[12:13], v11, off offset:16

.LBB0_37:
	s_or_b64 exec, exec, s[0:1]
	v_mov_b32_e32 v98, v97
	v_mov_b32_e32 v99, v97
	v_mov_b32_e32 v5, v97
	v_mov_b32_e32 v6, v97
	v_mov_b32_e32 v7, v97
	v_mov_b32_e32 v1, v97
	v_mov_b32_e32 v2, v97
	v_mov_b32_e32 v3, v97
	s_mov_b32 s0, 0x10000
	v_or_b32_e32 v8, 0x21000, v223
	v_mfma_f32_32x32x16_f16 v[32:47], v[96:99], v[0:3], 0
	v_mfma_f32_32x32x16_f16 v[16:31], v[4:7], v[0:3], 0
	v_or_b32_e32 v114, 0x21000, v223
	v_cmp_eq_u32_e64 s[0:1], 0, v225
	s_and_b64 vcc, vcc, s[0:1]
	ds_read_b128 v[8:11], v114
	ds_read_b128 v[12:15], v114 offset:32
	ds_read_b128 v[234:237], v114 offset:64
	ds_read_b128 v[238:241], v114 offset:96
	ds_read_b128 v[242:245], v114 offset:128
	ds_read_b128 v[106:109], v114 offset:160
	ds_read_b128 v[110:113], v114 offset:192
	s_waitcnt lgkmcnt(7)
	v_mfma_f32_32x32x16_f16 v[32:47], v[180:183], v[92:95], v[32:47]
	ds_read_b128 v[0:3], v114 offset:224
	v_mfma_f32_32x32x16_f16 v[32:47], v[184:187], v[88:91], v[32:47]
	v_mfma_f32_32x32x16_f16 v[32:47], v[188:191], v[84:87], v[32:47]
	v_mfma_f32_32x32x16_f16 v[32:47], v[192:195], v[80:83], v[32:47]
	v_mfma_f32_32x32x16_f16 v[32:47], v[196:199], v[76:79], v[32:47]
	v_mfma_f32_32x32x16_f16 v[32:47], v[200:203], v[72:75], v[32:47]
	v_mfma_f32_32x32x16_f16 v[32:47], v[204:207], v[68:71], v[32:47]
	v_mfma_f32_32x32x16_f16 v[32:47], v[208:211], v[64:67], v[32:47]
	s_waitcnt lgkmcnt(0)
	v_dot2c_f32_f16_e32 v98, v92, v8
	v_mfma_f32_32x32x16_f16 v[16:31], v[148:151], v[92:95], v[16:31]
	v_dot2c_f32_f16_e32 v98, v93, v9
	v_dot2c_f32_f16_e32 v98, v94, v10
	v_dot2c_f32_f16_e32 v98, v95, v11
	v_dot2c_f32_f16_e32 v98, v88, v12
	v_mfma_f32_32x32x16_f16 v[16:31], v[152:155], v[88:91], v[16:31]
	v_dot2c_f32_f16_e32 v98, v89, v13
	v_dot2c_f32_f16_e32 v98, v90, v14
	v_dot2c_f32_f16_e32 v98, v91, v15
	v_dot2c_f32_f16_e32 v98, v84, v234
	v_mfma_f32_32x32x16_f16 v[16:31], v[156:159], v[84:87], v[16:31]
	v_dot2c_f32_f16_e32 v98, v85, v235
	v_dot2c_f32_f16_e32 v98, v86, v236
	v_dot2c_f32_f16_e32 v98, v87, v237
	v_dot2c_f32_f16_e32 v98, v80, v238
	v_mfma_f32_32x32x16_f16 v[16:31], v[160:163], v[80:83], v[16:31]
	v_dot2c_f32_f16_e32 v98, v81, v239
	v_dot2c_f32_f16_e32 v98, v82, v240
	v_dot2c_f32_f16_e32 v98, v83, v241
	v_dot2c_f32_f16_e32 v98, v76, v242
	v_mfma_f32_32x32x16_f16 v[16:31], v[164:167], v[76:79], v[16:31]
	v_dot2c_f32_f16_e32 v98, v77, v243
	v_dot2c_f32_f16_e32 v98, v78, v244
	v_dot2c_f32_f16_e32 v98, v79, v245
	v_dot2c_f32_f16_e32 v98, v72, v106
	v_mfma_f32_32x32x16_f16 v[16:31], v[168:171], v[72:75], v[16:31]
	v_dot2c_f32_f16_e32 v98, v73, v107
	v_dot2c_f32_f16_e32 v98, v74, v108
	v_dot2c_f32_f16_e32 v98, v75, v109
	v_dot2c_f32_f16_e32 v98, v68, v110
	v_mfma_f32_32x32x16_f16 v[16:31], v[172:175], v[68:71], v[16:31]
	v_dot2c_f32_f16_e32 v98, v69, v111
	v_dot2c_f32_f16_e32 v98, v70, v112
	v_dot2c_f32_f16_e32 v98, v71, v113
	v_cvt_pk_f16_f32 v7, v38, v39
	v_cvt_pk_f16_f32 v6, v36, v37
	v_cvt_pk_f16_f32 v5, v34, v35
	v_cvt_pk_f16_f32 v4, v32, v33
	v_dot2c_f32_f16_e32 v98, v64, v0
	v_dot2c_f32_f16_e32 v98, v65, v1
	v_dot2c_f32_f16_e32 v98, v66, v2
	v_mfma_f32_32x32x16_f16 v[16:31], v[176:179], v[64:67], v[16:31]
	v_dot2c_f32_f16_e32 v98, v67, v3
	v_cvt_pk_f16_f32 v35, v46, v47
	v_cvt_pk_f16_f32 v34, v44, v45
	v_cvt_pk_f16_f32 v33, v42, v43
	v_cvt_pk_f16_f32 v32, v40, v41
	ds_bpermute_b32 v36, v102, v98
	v_cvt_f32_i32_e32 v37, v226
	v_mfma_f32_32x32x16_f16 v[0:15], v[4:7], v[60:63], 0
	s_nop 3
	v_cvt_pk_f16_f32 v23, v22, v23
	v_cvt_pk_f16_f32 v22, v20, v21
	v_cvt_pk_f16_f32 v21, v18, v19
	v_cvt_pk_f16_f32 v20, v16, v17
	v_cvt_pk_f16_f32 v19, v30, v31
	v_cvt_pk_f16_f32 v18, v28, v29
	v_cvt_pk_f16_f32 v17, v26, v27
	v_mfma_f32_32x32x16_f16 v[0:15], v[32:35], v[56:59], v[0:15]
	v_cvt_pk_f16_f32 v16, v24, v25
	s_waitcnt lgkmcnt(0)
	v_add_f32_e32 v36, v98, v36
	v_cvt_f16_f32_e32 v26, v100
	v_mov_b32_e32 v98, v97
	v_lshlrev_b32_e32 v32, 6, v218
	v_mfma_f32_32x32x16_f16 v[0:15], v[20:23], v[52:55], v[0:15]
	v_fma_mixlo_f16 v20, v37, v104, v36
	v_pack_b32_f16 v20, v20, 0
	v_pack_b32_f16 v21, v26, 0
	v_cndmask_b32_e32 v96, 0, v21, vcc
	v_mfma_f32_32x32x16_f16 v[0:15], v[16:19], v[48:51], v[0:15]
	v_cndmask_b32_e32 v16, 0, v20, vcc
	v_mov_b32_e32 v17, v97
	v_mov_b32_e32 v18, v97
	v_mov_b32_e32 v19, v97
	v_cmp_ne_u32_e32 vcc, 0, v225
	s_nop 0
	v_mfma_f32_32x32x16_f16 v[0:15], v[16:19], v[96:99], v[0:15]
	v_lshlrev_b32_e32 v70, 2, v215
	v_lshl_add_u32 v70, v214, 4, v70
	global_load_dwordx4 v[16:19], v70, s[2:3]
	global_load_dwordx4 v[20:23], v70, s[2:3] offset:32
	global_load_dwordx4 v[24:27], v70, s[2:3] offset:64
	global_load_dwordx4 v[28:31], v70, s[2:3] offset:96
	s_and_saveexec_b64 s[6:7], vcc
	s_cbranch_execz .LBB0_39
	v_lshl_or_b32 v71, v251, 12, v32
	v_add_u32_e32 v71, 0x18800, v71
	s_nop 7
	ds_write_b128 v71, v[0:3]
	ds_write_b128 v71, v[4:7] offset:16
	ds_write_b128 v71, v[8:11] offset:32
	ds_write_b128 v71, v[12:15] offset:48
.LBB0_39:
	s_or_b64 exec, exec, s[6:7]
	v_cvt_pk_f16_f32 v73, v118, v119
	v_cvt_pk_f16_f32 v72, v116, v117
	v_add_u32_e32 v76, v103, v105
	v_cvt_pk_f16_f32 v75, v122, v123
	v_cvt_pk_f16_f32 v74, v120, v121
	s_waitcnt lgkmcnt(0)
	s_barrier
	ds_write2_b64 v76, v[72:73], v[74:75] offset1:34
	v_cvt_pk_f16_f32 v73, v126, v127
	v_cvt_pk_f16_f32 v72, v124, v125
	v_cvt_pk_f16_f32 v75, v130, v131
	v_cvt_pk_f16_f32 v74, v128, v129
	ds_write2_b64 v76, v[72:73], v[74:75] offset0:68 offset1:102
	v_cvt_pk_f16_f32 v73, v134, v135
	v_cvt_pk_f16_f32 v72, v132, v133
	v_cvt_pk_f16_f32 v75, v138, v139
	v_cvt_pk_f16_f32 v74, v136, v137
	ds_write2_b64 v76, v[72:73], v[74:75] offset0:136 offset1:170
	v_cvt_pk_f16_f32 v73, v142, v143
	v_cvt_pk_f16_f32 v72, v140, v141
	v_cvt_pk_f16_f32 v75, v146, v147
	v_cvt_pk_f16_f32 v74, v144, v145
	ds_write2_b64 v76, v[72:73], v[74:75] offset0:204 offset1:238
	s_and_saveexec_b64 s[6:7], s[0:1]
	s_cbranch_execz .LBB0_49
	v_mov_b32_e32 v215, 0
	v_add_u32_e32 v54, v224, v223
	ds_read_b128 v[34:37], v54
	s_movk_i32 s0, 0x110
	v_mad_u32_u24 v70, v220, s0, v223
	ds_read_b128 v[38:41], v70 offset:34816
	ds_read_b128 v[42:45], v54 offset:32
	ds_read_b128 v[46:49], v70 offset:34848
	v_lshl_or_b32 v32, v251, 12, v32
	v_add_u32_e32 v78, 0x18800, v32
	v_div_scale_f32 v82, s[0:1], s10, s10, 1.0
	v_rcp_f32_e32 v84, v82
	v_div_scale_f32 v83, vcc, 1.0, s10, 1.0
	s_waitcnt vmcnt(0) lgkmcnt(2)
	v_mfma_f32_32x32x16_f16 v[16:31], v[34:37], v[38:41], v[16:31]
	ds_read_b128 v[34:37], v54 offset:64
	ds_read_b128 v[38:41], v70 offset:34880
	s_waitcnt lgkmcnt(2)
	v_mfma_f32_32x32x16_f16 v[16:31], v[42:45], v[46:49], v[16:31]
	ds_read_b128 v[42:45], v54 offset:96
	ds_read_b128 v[46:49], v70 offset:34912
	s_waitcnt lgkmcnt(2)
	v_mfma_f32_32x32x16_f16 v[16:31], v[34:37], v[38:41], v[16:31]
	ds_read_b128 v[32:35], v54 offset:128
	ds_read_b128 v[36:39], v54 offset:160
	ds_read_b128 v[50:53], v54 offset:192
	ds_read_b128 v[54:57], v54 offset:224
	ds_read_b128 v[58:61], v70 offset:34944
	ds_read_b128 v[62:65], v70 offset:34976
	ds_read_b128 v[66:69], v70 offset:35008
	ds_read_b128 v[70:73], v70 offset:35040
	s_waitcnt lgkmcnt(8)
	v_mfma_f32_32x32x16_f16 v[16:31], v[42:45], v[46:49], v[16:31]
	ds_read_b128 v[40:43], v78
	ds_read_b128 v[44:47], v78 offset:16
	ds_read_b128 v[74:77], v78 offset:32
	ds_read_b128 v[78:81], v78 offset:48
	v_fma_f32 v48, -v82, v84, 1.0
	v_fmac_f32_e32 v84, v48, v84
	v_mul_f32_e32 v48, v83, v84
	s_waitcnt lgkmcnt(7)
	v_mfma_f32_32x32x16_f16 v[16:31], v[32:35], v[58:61], v[16:31]
	s_waitcnt lgkmcnt(3)
	v_add_f32_e64 v32, v0, v40
	v_add_f32_e64 v33, v1, v41
	v_add_f32_e64 v0, v42, v2
	v_add_f32_e64 v1, v43, v3
	s_waitcnt lgkmcnt(2)
	v_pk_add_f32 v[2:3], v[4:5], v[44:45]
	v_pk_add_f32 v[4:5], v[46:47], v[6:7]
	s_waitcnt lgkmcnt(1)
	v_pk_add_f32 v[6:7], v[8:9], v[74:75]
	s_waitcnt lgkmcnt(0)
	v_pk_add_f32 v[8:9], v[12:13], v[78:79]
	v_fma_f32 v12, -v82, v48, v83
	v_mfma_f32_32x32x16_f16 v[16:31], v[36:39], v[62:65], v[16:31]
	v_fmac_f32_e32 v48, v12, v84
	v_cvt_pk_f16_f32 v2, v2, v3
	v_cvt_pk_f16_f32 v3, v4, v5
	v_cvt_pk_f16_f32 v1, v0, v1
	v_cvt_pk_f16_f32 v0, v32, v33
	v_fma_f32 v4, -v82, v48, v83
	v_div_fmas_f32 v4, v4, v84, v48
	v_mfma_f32_32x32x16_f16 v[16:31], v[50:53], v[66:69], v[16:31]
	v_add_f32_e64 v40, v76, v10
	v_add_f32_e64 v41, v77, v11
	v_add_f32_e64 v10, v80, v14
	v_add_f32_e64 v11, v81, v15
	v_div_fixup_f32 v4, v4, s10, 1.0
	v_cvt_pk_f16_f32 v34, v8, v9
	v_cvt_pk_f16_f32 v32, v6, v7
	v_cvt_pk_f16_f32 v35, v10, v11
	v_cvt_pk_f16_f32 v33, v40, v41
	v_mfma_f32_32x32x16_f16 v[16:31], v[54:57], v[70:73], v[16:31]
	s_andn2_b64 vcc, exec, s[8:9]
	s_nop 10
	v_mul_f32_e32 v8, v4, v16
	v_mul_f32_e32 v9, v4, v17
	v_mul_f32_e32 v5, v4, v18
	v_mul_f32_e32 v10, v4, v19
	v_mul_f32_e32 v6, v4, v20
	v_mul_f32_e32 v11, v4, v21
	v_mul_f32_e32 v7, v4, v22
	v_mul_f32_e32 v12, v4, v23
	v_mul_f32_e32 v16, v4, v24
	v_mul_f32_e32 v20, v4, v25
	v_mul_f32_e32 v17, v4, v26
	v_mul_f32_e32 v21, v4, v27
	v_mul_f32_e32 v18, v4, v28
	v_mul_f32_e32 v22, v4, v29
	v_mul_f32_e32 v19, v4, v30
	v_mul_f32_e32 v23, v4, v31
	v_cvt_pk_f16_f32 v7, v7, v12
	v_cvt_pk_f16_f32 v6, v6, v11
	v_cvt_pk_f16_f32 v5, v5, v10
	v_cvt_pk_f16_f32 v4, v8, v9
	v_cvt_pk_f16_f32 v19, v19, v23
	v_cvt_pk_f16_f32 v18, v18, v22
	v_mfma_f32_32x32x16_f16 v[0:15], v[0:3], v[4:7], 0
	v_cvt_pk_f16_f32 v17, v17, v21
	v_cvt_pk_f16_f32 v16, v16, v20
	s_nop 1
	v_mfma_f32_32x32x16_f16 v[0:15], v[32:35], v[16:19], v[0:15]
	s_cbranch_vccnz .LBB0_48
	v_lshlrev_b32_e32 v16, 7, v220
	v_lshl_or_b32 v16, v251, 12, v16
	v_mov_b32_e32 v17, v215
	s_add_i32 s33, s33, s46
	v_lshlrev_b32_e32 v22, 2, v214
	v_lshl_add_u64 v[16:17], v[16:17], 2, s[44:45]
	v_add_u32_e32 v18, s33, v214
	s_mov_b64 s[0:1], 0
	s_movk_i32 s10, 0x3fd
	v_mov_b32_e32 v23, v215
	s_branch .LBB0_43

.LBB0_48:
	s_nop 10
	v_cvt_pk_f16_f32 v7, v6, v7
	v_cvt_pk_f16_f32 v6, v4, v5
	v_cvt_pk_f16_f32 v4, v0, v1
	v_lshlrev_b32_e32 v0, 4, v218
	v_cvt_pk_f16_f32 v5, v2, v3
	v_lshl_or_b32 v16, v251, 11, v0
	v_cvt_pk_f16_f32 v3, v14, v15
	v_cvt_pk_f16_f32 v2, v12, v13
	v_cvt_pk_f16_f32 v1, v10, v11
	v_cvt_pk_f16_f32 v0, v8, v9
	ds_write_b128 v16, v[4:7] offset:43520
	ds_write_b128 v16, v[0:3] offset:44544
